# one static s_setprio 1 for waves 4-7 during GLA + hyena pre-pass and during the hyena Toeplitz convolution (reset to 0 at their ends)
# speedup vs baseline: 1.0091x; 1.0020x over previous
.LBB0_463:
	s_andn2_b64 vcc, exec, s[0:1]
	s_cbranch_vccnz .LBB0_748
	v_writelane_b32 v255, s86, 39
	s_movk_i32 s1, 0x800
	s_cmpk_gt_i32 s20, 0xff
	v_writelane_b32 v255, s87, 40
	v_writelane_b32 v255, s82, 43
	v_writelane_b32 v255, s94, 44
	s_cbranch_scc1 .LBB0_493
	s_add_u32 s78, s76, 0x46600000
	s_addc_u32 s79, s77, 0
	s_add_u32 s80, s76, 0x15e00000
	s_addc_u32 s81, s77, 0
	s_lshl_b32 s82, s71, 3
	s_or_b32 s84, s82, 1
	s_sub_i32 s83, 0xff, s82
	s_sub_i32 s85, 0xff, s84
	s_lshl_b32 s86, s71, 8
	s_cmp_gt_i32 s71, 0
	s_waitcnt lgkmcnt(0)
	s_cselect_b64 s[42:43], -1, 0
	s_cmp_gt_i32 s71, 1
	s_cselect_b64 s[44:45], -1, 0
	s_cmp_gt_i32 s71, 2
	s_waitcnt vmcnt(0)
	v_ashrrev_i32_e32 v17, 3, v126
	s_cselect_b64 s[46:47], -1, 0
	s_cmp_gt_i32 s71, 3
	v_and_b32_e32 v86, 0x7f, v126
	v_and_b32_e32 v87, -16, v17
	v_lshl_add_u32 v91, v127, 2, 0
	v_lshlrev_b32_e32 v3, 1, v127
	s_cselect_b64 s[48:49], -1, 0
	s_cmp_gt_i32 s71, 4
	v_and_b32_e32 v1, 15, v126
	v_lshrrev_b32_e32 v2, 4, v127
	v_sub_u32_e32 v92, v91, v3
	v_mul_u32_u24_e32 v3, 0x90, v86
	v_lshlrev_b32_e32 v4, 1, v87
	s_cselect_b64 s[50:51], -1, 0
	s_cmp_gt_i32 s71, 5
	s_movk_i32 s0, 0x8e
	v_add3_u32 v94, 0, v3, v4
	v_lshlrev_b32_e32 v4, 3, v2
	v_lshlrev_b32_e32 v2, 2, v2
	v_lshlrev_b32_e32 v6, 4, v126
	v_mul_u32_u24_e32 v100, 0x90, v1
	s_cselect_b64 s[52:53], -1, 0
	s_cmp_gt_i32 s71, 6
	v_mad_u32_u24 v93, v127, s0, v92
	v_sub_u32_e32 v2, v1, v2
	v_and_b32_e32 v76, 0x70, v6
	s_movk_i32 s0, 0x110
	v_add3_u32 v101, 0, v100, v4
	s_cselect_b64 s[54:55], -1, 0
	s_cmp_gt_i32 s71, 7
	v_and_b32_e32 v5, 48, v127
	v_mul_lo_u32 v6, v17, s0
	v_lshlrev_b32_e32 v7, 1, v76
	v_cmp_gt_i32_e32 vcc, 0, v2
	v_cmp_gt_i32_e64 s[58:59], 1, v2
	v_cmp_gt_i32_e64 s[62:63], 2, v2
	v_cmp_gt_i32_e64 s[40:41], 3, v2
	v_lshlrev_b32_e32 v2, 7, v1
	v_add_u32_e32 v103, 0x1200, v101
	s_movk_i32 s0, 0x1000
	s_cselect_b64 s[56:57], -1, 0
	s_lshl_b32 s87, s71, 4
	v_add_u32_e32 v95, 0, v5
	v_add3_u32 v96, 0, v6, v7
	v_mul_u32_u24_e32 v6, 0x48, v1
	v_add_u32_e32 v102, 0x900, v101
	v_add3_u32 v8, v103, v2, s0
	v_add_u32_e32 v104, 0x1b00, v101
	s_movk_i32 s0, 0x1800
	s_cmp_lt_u32 s16, 64
	v_lshl_add_u32 v97, v6, 1, v95
	v_add_u32_e32 v6, v101, v2
	v_add3_u32 v7, v102, v2, s1
	v_add3_u32 v2, v104, v2, s0
	s_cselect_b64 s[18:19], -1, 0
	v_or_b32_e32 v1, s87, v1
	s_movk_i32 s0, 0x90
	s_and_b64 s[62:63], s[40:41], s[62:63]
	v_or_b32_e32 v89, 1, v87
	v_mul_i32_i24_e32 v3, 0xffffff74, v127
	v_and_b32_e32 v5, 48, v126
	v_mul_lo_u32 v105, v1, s0
	s_lshl_b32 s0, s71, 5
	s_and_b64 s[72:73], s[62:63], s[58:59]
	v_sub_u32_e32 v88, 0xff, v87
	v_sub_u32_e32 v90, 0xff, v89
	v_mov_b32_e32 v77, v34
	v_add_u32_e32 v98, 0x1200, v97
	v_add_u32_e32 v99, 0x1b00, v97
	v_add3_u32 v106, 0, v105, v4
	v_sub_u32_e32 v107, 0, v17
	v_lshrrev_b32_e32 v218, 4, v127
	v_lshl_add_u32 v218, v218, 2, s87
	s_sub_i32 s16, 0, s82
	v_sub_u32_e32 v108, 0, v87
	v_add_u32_e32 v109, v93, v3
	v_add_u32_e32 v110, s0, v6
	v_add_u32_e32 v111, s0, v7
	v_add_u32_e32 v112, s0, v8
	v_add_u32_e32 v113, s0, v2
	v_add_u32_e32 v114, 0, v5
	s_and_b64 s[2:3], s[72:73], vcc
	s_mov_b32 s17, s20
	s_cmp_ge_u32 s71, 4
	s_cbranch_scc0 .Lprio_gla
	s_setprio 1
.Lprio_gla:
	s_branch .LBB0_467

.LBB0_748:
	s_setprio 0
	s_mul_i32 s0, s24, 9
	v_readlane_b32 s76, v254, 7
	s_add_i32 s16, s0, 4
	v_readlane_b32 s77, v254, 8
	s_cmp_lt_i32 s16, s77
	v_readlane_b32 s2, v254, 9
	s_cselect_b64 s[0:1], -1, 0
	v_readlane_b32 s3, v254, 10
	s_and_b64 s[0:1], s[2:3], s[0:1]
	s_andn2_b64 vcc, exec, s[0:1]
	s_cbranch_vccnz .LBB0_760
	s_waitcnt vmcnt(0)
	s_waitcnt vmcnt(0) lgkmcnt(0)
	s_barrier
	s_mov_b64 s[2:3], exec
	v_readlane_b32 s0, v255, 23
	v_readlane_b32 s1, v255, 24
	s_and_b64 s[0:1], s[2:3], s[0:1]
	v_readlane_b32 s71, v255, 36
	s_mov_b64 exec, s[0:1]
	s_cbranch_execz .LBB0_798
	v_mov_b32_e32 v1, s83
	s_waitcnt vmcnt(0) expcnt(0) lgkmcnt(0)
	ds_read_b32 v3, v1
	ds_read_b32 v2, v1 offset:4
	s_waitcnt lgkmcnt(1)
	v_cmp_ne_u32_e32 vcc, 0, v3
	s_cbranch_vccnz .LBB0_766
	v_readlane_b32 s14, v254, 0
	v_readlane_b32 s15, v254, 1
	s_load_dwordx2 s[0:1], s[14:15], 0x4
	s_mov_b32 s20, 1
	s_waitcnt lgkmcnt(0)
	s_mul_i32 s17, s0, s68
	s_mul_i32 s17, s17, s1
	s_branch .LBB0_753

.LBB0_801:
	s_andn2_b64 vcc, exec, s[0:1]
	s_cbranch_vccnz .LBB0_874
	s_mov_b32 s0, 0
	s_add_i32 s28, s0, s84
	s_waitcnt vmcnt(0)
	v_add_u32_e32 v2, s0, v0
	s_cmpk_gt_i32 s28, 0x23f
	v_readfirstlane_b32 s1, v2
	s_cbranch_scc1 .LBB0_823
	s_ashr_i32 s36, s1, 6
	s_ashr_i32 s1, s0, 31
	v_readlane_b32 s2, v254, 2
	v_readlane_b32 s3, v254, 3
	s_add_u32 s2, s2, s0
	s_addc_u32 s3, s3, s1
	s_add_u32 s14, s2, 0x32600000
	s_addc_u32 s15, s3, 0
	s_lshr_b64 s[16:17], s[24:25], 1
	s_lshr_b32 s17, s25, 1
	s_mul_i32 s17, s17, 0x480000
	s_mul_hi_u32 s18, s16, 0x480000
	s_mul_i32 s45, s16, 0x480000
	s_lshl_b32 s16, s36, 8
	s_add_i32 s20, s18, s17
	s_lshl_b32 s37, s82, 9
	s_lshl_b32 s46, s36, 10
	s_not_b32 s47, s16
	s_lshl_b64 s[18:19], s[0:1], 3
	s_waitcnt lgkmcnt(0)
	v_readlane_b32 s42, v254, 4
	v_readlane_b32 s43, v254, 5
	s_add_u32 s18, s42, s18
	v_bfe_u32 v1, v2, 5, 1
	s_addc_u32 s19, s43, s19
	v_and_b32_e32 v165, 31, v2
	v_lshlrev_b32_e32 v218, 3, v1
	v_mov_b32_e32 v219, v34
	v_lshlrev_b32_e32 v4, 4, v1
	v_mov_b32_e32 v5, v34
	s_movk_i32 s17, 0x200
	s_load_dwordx2 s[42:43], s[18:19], 0xc8
	s_mul_i32 s18, s36, 0x4200
	v_mul_u32_u24_e32 v3, 0x140, v165
	v_lshl_add_u64 v[220:221], s[14:15], 0, v[4:5]
	v_cmp_gt_i32_e64 s[40:41], s17, v2
	s_add_i32 s17, s18, 0
	v_lshl_add_u64 v[222:223], s[14:15], 0, v[218:219]
	v_lshl_add_u64 v[6:7], s[2:3], 0, v[218:219]
	s_mov_b64 s[14:15], 0x41600000
	v_or_b32_e32 v214, 0x2110000, v3
	v_mov_b32_e32 v3, s17
	s_ashr_i32 s17, s16, 31
	v_lshl_add_u64 v[224:225], v[6:7], 0, s[14:15]
	v_readlane_b32 s14, v255, 9
	v_add_u32_e32 v167, s0, v217
	s_add_u32 s14, s14, s0
	v_readlane_b32 s0, v255, 10
	s_movk_i32 s19, 0x210
	s_addc_u32 s15, s0, s1
	v_mad_u32_u24 v8, v165, s19, v3
	v_ashrrev_i32_e32 v3, 31, v2
	s_add_u32 s0, s14, s45
	v_lshl_add_u32 v219, v2, 4, 0
	v_lshlrev_b64 v[2:3], 4, v[2:3]
	s_addc_u32 s1, s15, s20
	v_lshl_add_u64 v[226:227], s[0:1], 0, v[2:3]
	s_lshl_b32 s0, s28, 3
	s_ashr_i32 s29, s28, 31
	s_add_i32 s44, s0, 0xfffff000
	s_lshl_b64 s[0:1], s[28:29], 13
	s_add_u32 s0, s45, s0
	s_addc_u32 s1, s20, s1
	s_add_u32 s0, s14, s0
	s_addc_u32 s1, s15, s1
	v_lshlrev_b32_e32 v4, 4, v165
	v_lshl_add_u64 v[228:229], s[0:1], 0, v[2:3]
	s_movk_i32 s0, 0x1080
	v_mad_u64_u32 v[2:3], s[0:1], v1, s0, v[4:5]
	s_lshl_b64 s[0:1], s[16:17], 1
	s_add_u32 s0, s2, s0
	s_addc_u32 s1, s3, s1
	v_lshl_add_u64 v[230:231], s[0:1], 0, v[2:3]
	v_mov_b32_e32 v2, s18
	v_mad_u32_u24 v1, v1, s19, v2
	v_mov_b32_e32 v215, v34
	v_mul_u32_u24_e32 v216, 0x840, v165
	v_add3_u32 v246, v1, v4, 0
	v_add_u32_e32 v247, v8, v218
	s_cmp_ge_u32 s36, 4
	s_cbranch_scc0 .Lprio_hyc
	s_setprio 1

.LBB0_823:
	s_setprio 0
	s_mul_i32 s0, s24, 9
	s_add_i32 s16, s0, 5
	s_cmp_lt_i32 s16, s77
	v_readlane_b32 s2, v254, 9
	s_cselect_b64 s[0:1], -1, 0
	v_readlane_b32 s3, v254, 10
	s_and_b64 s[0:1], s[2:3], s[0:1]
	s_andn2_b64 vcc, exec, s[0:1]
	s_waitcnt lgkmcnt(0)
	s_barrier
	s_cbranch_vccnz .LBB0_835
	s_waitcnt vmcnt(0)
	s_barrier
	s_mov_b64 s[2:3], exec
	v_readlane_b32 s0, v255, 23
	v_readlane_b32 s1, v255, 24
	v_readlane_b32 s44, v255, 28
	v_readlane_b32 s46, v255, 37
	s_and_b64 s[0:1], s[2:3], s[0:1]
	v_readlane_b32 s45, v255, 29
	v_readlane_b32 s47, v255, 38
	s_mov_b64 exec, s[0:1]
	s_cbranch_execz .LBB0_873
	v_mov_b32_e32 v1, s83
	s_waitcnt vmcnt(0) expcnt(0) lgkmcnt(0)
	ds_read_b32 v3, v1
	ds_read_b32 v2, v1 offset:4
	s_waitcnt lgkmcnt(1)
	v_cmp_ne_u32_e32 vcc, 0, v3
	s_cbranch_vccnz .LBB0_841
	v_readlane_b32 s14, v254, 0
	v_readlane_b32 s15, v254, 1
	s_load_dwordx2 s[0:1], s[14:15], 0x4
	s_mov_b32 s20, 1
	s_waitcnt lgkmcnt(0)
	s_mul_i32 s17, s0, s68
	s_mul_i32 s17, s17, s1
	s_branch .LBB0_828
